# v39 + thin2 -> gate/up GEMM grid barrier replaced by per-token-tile counters (kept global for the last mixer)
# baseline (speedup 1.0000x reference)
; __device__ __forceinline__ unsigned xb_ld(unsigned* p)              { return __hip_atomic_load(p, __ATOMIC_RELAXED, __HIP_MEMORY_SCOPE_AGENT); }
; __device__ __forceinline__ unsigned xb_add(unsigned* p, unsigned v) { return __hip_atomic_fetch_add(p, v, __ATOMIC_RELAXED, __HIP_MEMORY_SCOPE_AGENT); }
; #define XB_SPIN(cond, bar) do { unsigned _sp = 0; while (cond) { __builtin_amdgcn_s_sleep(1); \
;     if ((++_sp & 255u) == 0u) { if (xb_ld(&(bar)[XB_TMO])) break; if (_sp > XB_SPIN_CAP) { atomicAdd(&(bar)[XB_TMO], 1u); break; } } } } while (0)
; __device__ __forceinline__ void xcd_barrier(const XcdBarrier& b) {
;     asm volatile("s_waitcnt vmcnt(0)" ::: "memory");
;     __syncthreads();
;     if (threadIdx.x == 0) {
;         unsigned* bar = b.bar;
;         __builtin_amdgcn_s_waitcnt(0);
;         unsigned nloc = b.st[0], nx = b.st[1];
;         if (nloc == 0u) { xcd_barrier_complete(bar, b.x, nloc, nx); b.st[0] = nloc; b.st[1] = nx; }
;         const unsigned old = xb_add(&bar[XB_XSUB(b.x)], 1u);
;         const unsigned gen = old / nloc;
;         if (old + 1u == (gen + 1u) * nloc) {
;             __builtin_amdgcn_fence(__ATOMIC_RELEASE, "agent");
;             asm volatile("s_waitcnt vmcnt(0)" ::: "memory");
;             const unsigned og = xb_add(&bar[XB_TOP], 1u);
;             const unsigned tg = og / nx;
;             if (og + 1u == (tg + 1u) * nx) xb_add(&bar[XB_TOPGEN], 1u);
;             else XB_SPIN(xb_ld(&bar[XB_TOPGEN]) == tg, bar);
;             __builtin_amdgcn_fence(__ATOMIC_ACQUIRE, "agent");
;             xb_add(&bar[XB_XGEN(b.x)], 1u);
;             asm volatile("s_waitcnt vmcnt(0)" ::: "memory");
;         } else {
;             XB_SPIN(xb_ld(&bar[XB_XGEN(b.x)]) == gen, bar);
;             __builtin_amdgcn_fence(__ATOMIC_ACQUIRE, "agent");
;             asm volatile("s_waitcnt vmcnt(0)" ::: "memory");
;         }
;     }
;     __syncthreads();
; }
.LBB0_1759:
	v_readlane_b32 s34, v253, 36
	v_readlane_b32 s35, v253, 37
	s_mov_b32 s0, s76
	s_waitcnt vmcnt(0)
	s_waitcnt lgkmcnt(0)
	s_barrier
	s_mov_b64 s[36:37], exec
	v_readlane_b32 s2, v253, 53
	v_readlane_b32 s3, v253, 54
	s_and_b64 s[2:3], s[36:37], s[2:3]
	s_mov_b64 exec, s[2:3]
	s_cbranch_execz .LBB0_1803
	v_readlane_b32 s14, v253, 55
	s_nop 3
	s_cmp_eq_u32 s14, 6
	s_cbranch_scc1 .Lth_old_LBB0_1803
	v_readlane_b32 s10, v253, 36
	v_readlane_b32 s11, v253, 37
	v_readlane_b32 s14, v253, 55
	s_nop 3
	s_add_u32 s12, s10, 0x7000
	s_addc_u32 s13, s11, 0
	s_and_b32 s15, s88, 7
	s_lshr_b32 s16, s88, 3
	s_lshl_b32 s15, s15, 3
	s_and_b32 s17, s16, 7
	s_add_i32 s17, s17, s15
	s_lshr_b32 s16, s16, 2
	s_add_i32 s16, s16, s15
	s_lshl_b32 s17, s17, 6
	s_lshl_b32 s16, s16, 6
	s_mov_b32 s19, s16
	s_mov_b32 s16, s17
	s_mov_b32 s17, s19
	s_lshr_b32 s14, s14, 1
	s_add_i32 s14, s14, 1
	s_lshl_b32 s14, s14, 2
	v_mov_b32_e32 v2, s17
	v_mov_b32_e32 v5, 1
	v_mov_b32_e32 v4, s16
	global_atomic_add v2, v5, s[12:13]
	s_mov_b32 s18, 0

; __device__ __forceinline__ unsigned xb_add(unsigned* p, unsigned v) { return __hip_atomic_fetch_add(p, v, __ATOMIC_RELAXED, __HIP_MEMORY_SCOPE_AGENT); }
; __device__ __forceinline__ void xcd_barrier(const XcdBarrier& b) {
;     ...
;     if (threadIdx.x == 0) {
;         unsigned* bar = b.bar;
;         __builtin_amdgcn_s_waitcnt(0);
;         unsigned nloc = b.st[0], nx = b.st[1];
;         if (nloc == 0u) { xcd_barrier_complete(bar, b.x, nloc, nx); b.st[0] = nloc; b.st[1] = nx; }
;         const unsigned old = xb_add(&bar[XB_XSUB(b.x)], 1u);
.Lth_done_LBB0_1803:
	buffer_inv sc1
	s_waitcnt vmcnt(0)
	s_branch .LBB0_1803
.Lth_old_LBB0_1803:
	v_mov_b32_e32 v2, s77
	s_waitcnt vmcnt(0) expcnt(0) lgkmcnt(0)
	ds_read_b32 v4, v2
	ds_read_b32 v2, v2 offset:4
	s_waitcnt lgkmcnt(1)
	v_cmp_ne_u32_e32 vcc, 0, v4
	s_cbranch_vccnz .LBB0_1774
	v_readlane_b32 s2, v253, 38
	v_readlane_b32 s3, v253, 39
	s_load_dwordx2 s[6:7], s[2:3], 0x0
	s_load_dword s1, s[2:3], 0x8
	s_add_u32 s2, s34, 0x1000
	s_addc_u32 s3, s35, 0
	s_add_u32 s4, s34, 0x1100
	s_waitcnt lgkmcnt(0)
	s_mul_i32 s5, s7, s6
	s_mul_i32 s1, s5, s1
	s_addc_u32 s5, s35, 0
	s_add_u32 s6, s34, 0x1200
	s_addc_u32 s7, s35, 0
	s_add_u32 s8, s34, 0x1300
	s_addc_u32 s9, s35, 0
	s_mov_b32 s28, 1
	s_mov_b64 s[10:11], 0
	s_branch .LBB0_1764
